# speedup vs baseline: 1.0391x; 1.0072x over previous
.LBB4_18:
.LBB4_24:
	s_and_b64 s[50:51], s[42:43], exec
	s_cselect_b32 s52, s39, s47
	s_cselect_b32 s53, s38, s46
	s_cselect_b32 s54, s41, s45
	s_cselect_b32 s55, s40, s44
	s_add_u32 s28, s46, 0x100
	s_addc_u32 s84, s47, 0
	s_and_b64 s[50:51], s[48:49], exec
	s_cselect_b32 s51, s52, s84
	s_cselect_b32 s50, s53, s28
	s_add_u32 s28, s44, 0x100
	s_addc_u32 s84, s45, 0
	s_and_b64 s[48:49], s[48:49], exec
	s_cselect_b32 s49, s54, s84
	s_cselect_b32 s48, s55, s28
	s_mov_b32 m0, s59
	v_add_u32_e32 v229, s76, v234
	v_lshl_add_u64 v[130:131], s[48:49], 0, v[216:217]
	ds_read_b128 v[74:77], v229
	ds_read_b128 v[86:89], v229 offset:1024
	ds_read_b128 v[98:101], v229 offset:2048
	ds_read_b128 v[106:109], v229 offset:3072
	global_load_lds_dwordx4 v[130:131], off
	v_lshl_add_u64 v[132:133], s[48:49], 0, v[218:219]
	s_mov_b32 m0, s60
	s_nop 0
	global_load_lds_dwordx4 v[132:133], off
	s_barrier
	s_waitcnt lgkmcnt(0)
	s_setprio 1
	s_waitcnt lgkmcnt(0)
	v_mfma_f32_16x16x32_f16 v[94:97], v[74:77], v[46:49], 0
	v_mfma_f32_16x16x32_f16 v[46:49], v[98:101], v[46:49], 0
	v_mfma_f32_16x16x32_f16 v[94:97], v[86:89], v[50:53], v[94:97]
	v_mfma_f32_16x16x32_f16 v[50:53], v[106:109], v[50:53], v[46:49]
	v_mfma_f32_16x16x32_f16 v[46:49], v[74:77], v[38:41], 0
	v_mfma_f32_16x16x32_f16 v[38:41], v[98:101], v[38:41], 0
	v_mfma_f32_16x16x32_f16 v[110:113], v[106:109], v[42:45], v[38:41]
	v_mfma_f32_16x16x32_f16 v[38:41], v[74:77], v[30:33], 0
	v_mfma_f32_16x16x32_f16 v[30:33], v[98:101], v[30:33], 0
	v_mfma_f32_16x16x32_f16 v[174:177], v[106:109], v[34:37], v[30:33]
	v_mfma_f32_16x16x32_f16 v[30:33], v[74:77], v[22:25], 0
	v_mfma_f32_16x16x32_f16 v[22:25], v[98:101], v[22:25], 0
	v_mfma_f32_16x16x32_f16 v[102:105], v[86:89], v[42:45], v[46:49]
	v_mfma_f32_16x16x32_f16 v[170:173], v[86:89], v[34:37], v[38:41]
	v_mfma_f32_16x16x32_f16 v[178:181], v[86:89], v[26:29], v[30:33]
	v_mfma_f32_16x16x32_f16 v[182:185], v[106:109], v[26:29], v[22:25]
	s_setprio 0
	s_mov_b32 m0, s58
	s_barrier
	ds_read_b128 v[34:37], v237 offset:16384
	ds_read_b128 v[46:49], v237 offset:17408
	ds_read_b128 v[114:117], v237 offset:18432
	ds_read_b128 v[118:121], v237 offset:19456
	ds_read_b128 v[122:125], v237 offset:20480
	ds_read_b128 v[126:129], v237 offset:21504
	ds_read_b128 v[166:169], v237 offset:22528
	ds_read_b128 v[186:189], v237 offset:23552
	global_load_lds_dwordx4 v220, s[50:51]
	s_mov_b32 m0, s62
	s_nop 0
	global_load_lds_dwordx4 v226, s[50:51]
	s_barrier
	s_waitcnt lgkmcnt(0)
	s_setprio 1
	s_waitcnt lgkmcnt(0)
	v_mfma_f32_16x16x32_f16 v[22:25], v[6:9], v[34:37], 0
	v_mfma_f32_16x16x32_f16 v[30:33], v[6:9], v[114:117], 0
	v_mfma_f32_16x16x32_f16 v[42:45], v[6:9], v[122:125], 0
	v_mfma_f32_16x16x32_f16 v[6:9], v[6:9], v[166:169], 0
	v_mfma_f32_16x16x32_f16 v[22:25], v[10:13], v[46:49], v[22:25]
	v_mfma_f32_16x16x32_f16 v[26:29], v[14:17], v[34:37], 0
	v_mfma_f32_16x16x32_f16 v[30:33], v[10:13], v[118:121], v[30:33]
	v_mfma_f32_16x16x32_f16 v[38:41], v[14:17], v[114:117], 0
	v_mfma_f32_16x16x32_f16 v[42:45], v[10:13], v[126:129], v[42:45]
	v_mfma_f32_16x16x32_f16 v[134:137], v[14:17], v[122:125], 0
	v_mfma_f32_16x16x32_f16 v[6:9], v[10:13], v[186:189], v[6:9]
	v_mfma_f32_16x16x32_f16 v[10:13], v[14:17], v[166:169], 0
	v_mfma_f32_16x16x32_f16 v[26:29], v[18:21], v[46:49], v[26:29]
	v_mfma_f32_16x16x32_f16 v[38:41], v[18:21], v[118:121], v[38:41]
	v_mfma_f32_16x16x32_f16 v[134:137], v[18:21], v[126:129], v[134:137]
	v_mfma_f32_16x16x32_f16 v[14:17], v[18:21], v[186:189], v[10:13]
	s_setprio 0
	s_barrier
	s_add_u32 s86, s48, 0x40000
	s_addc_u32 s87, s49, 0
	s_add_i32 s84, s76, s57
	v_lshl_add_u64 v[10:11], s[86:87], 0, v[216:217]
	s_mov_b32 m0, s84
	s_add_i32 s85, s84, 0x2000
	global_load_lds_dwordx4 v[10:11], off
	v_lshl_add_u64 v[10:11], s[86:87], 0, v[218:219]
	s_mov_b32 m0, s85
	s_nop 0
	global_load_lds_dwordx4 v[10:11], off
	s_add_i32 s94, s61, s33
	s_mov_b32 s95, 0
	s_cmpk_gt_u32 s94, 0x15ff
	s_cselect_b64 s[96:97], -1, 0
	s_and_b64 s[96:97], s[96:97], exec
	s_cselect_b32 s96, 0x7fffea00, 0
	s_cselect_b32 s98, s25, s15
	s_cselect_b32 s99, s24, s14
	s_add_i32 s96, s96, s94
	s_lshl_b32 s94, s96, 1
	s_addk_i32 s94, 0x2c00
	s_lshl_b64 s[96:97], s[94:95], 12
	s_add_u32 s100, s99, s96
	s_addc_u32 s101, s98, s97
	s_add_i32 s94, s75, s61
	s_cmpk_gt_u32 s94, 0x15ff
	s_cselect_b32 s97, 0x7fffea00, 0
	s_cselect_b32 s96, 0x80, 0
	s_add_i32 s97, s97, s94
	s_lshl_b32 s94, s97, 1
	s_add_i32 s97, s94, 0x2c00
	s_mul_hi_u32 s98, s97, 0xba2e8ba3
	s_lshr_b32 s98, s98, 11
	s_mul_i32 s99, s98, 0x7ffff500
	s_add_i32 s99, s99, s97
	s_lshr_b32 s97, s99, 7
	s_mul_i32 s98, s98, 22
	s_add_i32 s97, s97, s98
	s_lshl_b32 s97, s97, 8
	s_and_b32 s94, s94, 0x7e
	s_or_b32 s96, s97, s96
	s_or_b32 s94, s96, s94
	s_lshl_b64 s[96:97], s[94:95], 11
	s_waitcnt vmcnt(6)
	s_cmp_gt_i32 s61, 44
	s_cbranch_scc1 .Lhka_done_a0
	s_cmp_lt_i32 s61, 1
	s_cbranch_scc1 .Lhka_ld_a0
	v_cvt_pk_f16_f32 v2, v2, v3
	v_cvt_pk_f16_f32 v3, v4, v5
	v_lshl_add_u64 v[4:5], v[224:225], 0, s[96:97]
	global_store_dwordx2 v[4:5], v[2:3], off
.Lhka_ld_a0:
	s_cmp_eq_u32 s61, 44
	s_cbranch_scc1 .Lhka_inc_a0
	v_lshlrev_b32_e32 v4, 2, v214
	v_mov_b32_e32 v5, v221
	v_lshl_add_u64 v[4:5], s[100:101], 0, v[4:5]
	global_load_dwordx4 v[2:5], v[4:5], off nt

.LBB4_30:
	v_mov_b32_e32 v227, v221
	v_lshl_add_u64 v[54:55], s[50:51], 0, v[220:221]
	v_lshl_add_u64 v[56:57], s[50:51], 0, v[226:227]
	s_add_i32 s50, 0, 0x1c000
	s_mov_b32 m0, s67
	v_add_u32_e32 v238, s50, v234
	v_lshl_add_u64 v[58:59], v[130:131], 0, s[30:31]
	ds_read_b128 v[240:243], v238
	ds_read_b128 v[244:247], v238 offset:1024
	ds_read_b128 v[248:251], v238 offset:2048
	ds_read_b128 v[252:255], v238 offset:3072
	global_load_lds_dwordx4 v[58:59], off
	v_lshl_add_u64 v[58:59], v[132:133], 0, s[30:31]
	s_mov_b32 m0, s68
	s_nop 0
	global_load_lds_dwordx4 v[58:59], off
	s_barrier
	s_waitcnt lgkmcnt(0)
	s_setprio 1
	s_waitcnt lgkmcnt(0)
	v_mfma_f32_16x16x32_f16 v[58:61], v[240:243], v[122:125], v[94:97]
	v_mfma_f32_16x16x32_f16 v[50:53], v[248:251], v[122:125], v[50:53]
	v_mfma_f32_16x16x32_f16 v[130:133], v[244:247], v[126:129], v[58:61]
	v_mfma_f32_16x16x32_f16 v[126:129], v[252:255], v[126:129], v[50:53]
	v_mfma_f32_16x16x32_f16 v[50:53], v[240:243], v[118:121], v[102:105]
	v_mfma_f32_16x16x32_f16 v[122:125], v[244:247], v[210:213], v[50:53]
	v_mfma_f32_16x16x32_f16 v[50:53], v[248:251], v[118:121], v[110:113]
	v_mfma_f32_16x16x32_f16 v[118:121], v[252:255], v[210:213], v[50:53]
	v_mfma_f32_16x16x32_f16 v[50:53], v[240:243], v[202:205], v[170:173]
	v_mfma_f32_16x16x32_f16 v[110:113], v[244:247], v[206:209], v[50:53]
	v_mfma_f32_16x16x32_f16 v[50:53], v[248:251], v[202:205], v[174:177]
	v_mfma_f32_16x16x32_f16 v[102:105], v[252:255], v[206:209], v[50:53]
	v_mfma_f32_16x16x32_f16 v[50:53], v[240:243], v[18:21], v[178:181]
	v_mfma_f32_16x16x32_f16 v[18:21], v[248:251], v[18:21], v[182:185]
	v_mfma_f32_16x16x32_f16 v[94:97], v[244:247], v[198:201], v[50:53]
	v_mfma_f32_16x16x32_f16 v[82:85], v[252:255], v[198:201], v[18:21]
	s_setprio 0
	s_mov_b32 m0, s69
	s_nop 3
	v_lshl_add_u64 v[18:19], v[54:55], 0, s[30:31]
	s_barrier
	ds_read_b128 v[66:69], v237 offset:49152
	ds_read_b128 v[78:81], v237 offset:50176
	ds_read_b128 v[170:173], v237 offset:51200
	ds_read_b128 v[174:177], v237 offset:52224
	ds_read_b128 v[178:181], v237 offset:53248
	ds_read_b128 v[182:185], v237 offset:54272
	ds_read_b128 v[198:201], v237 offset:55296
	ds_read_b128 v[202:205], v237 offset:56320
	global_load_lds_dwordx4 v[18:19], off
	v_lshl_add_u64 v[18:19], v[56:57], 0, s[30:31]
	s_mov_b32 m0, s70
	s_nop 0
	global_load_lds_dwordx4 v[18:19], off
	s_barrier
	s_waitcnt lgkmcnt(0)
	s_setprio 1
	s_waitcnt lgkmcnt(0)
	v_mfma_f32_16x16x32_f16 v[18:21], v[10:13], v[66:69], v[22:25]
	v_mfma_f32_16x16x32_f16 v[70:73], v[186:189], v[78:81], v[18:21]
	v_mfma_f32_16x16x32_f16 v[18:21], v[190:193], v[66:69], v[26:29]
	v_mfma_f32_16x16x32_f16 v[58:61], v[194:197], v[78:81], v[18:21]
	v_mfma_f32_16x16x32_f16 v[18:21], v[10:13], v[170:173], v[30:33]
	v_mfma_f32_16x16x32_f16 v[50:53], v[186:189], v[174:177], v[18:21]
	v_mfma_f32_16x16x32_f16 v[18:21], v[190:193], v[170:173], v[38:41]
	v_mfma_f32_16x16x32_f16 v[38:41], v[194:197], v[174:177], v[18:21]
	v_mfma_f32_16x16x32_f16 v[18:21], v[10:13], v[178:181], v[42:45]
	v_mfma_f32_16x16x32_f16 v[6:9], v[10:13], v[198:201], v[6:9]
	v_mfma_f32_16x16x32_f16 v[26:29], v[186:189], v[182:185], v[18:21]
	v_mfma_f32_16x16x32_f16 v[18:21], v[190:193], v[178:181], v[134:137]
	v_mfma_f32_16x16x32_f16 v[10:13], v[186:189], v[202:205], v[6:9]
	v_mfma_f32_16x16x32_f16 v[6:9], v[190:193], v[198:201], v[14:17]
	v_mfma_f32_16x16x32_f16 v[18:21], v[194:197], v[182:185], v[18:21]
	v_mfma_f32_16x16x32_f16 v[6:9], v[194:197], v[202:205], v[6:9]
	s_setprio 0
	s_barrier
	s_add_u32 s48, s48, 0x40080
	s_addc_u32 s49, s49, 0
	s_add_i32 s50, s50, s57
	v_lshl_add_u64 v[14:15], s[48:49], 0, v[216:217]
	s_mov_b32 m0, s50
	s_add_i32 s51, s50, 0x2000
	global_load_lds_dwordx4 v[14:15], off
	v_lshl_add_u64 v[14:15], s[48:49], 0, v[218:219]
	s_mov_b32 m0, s51
	s_nop 0
	global_load_lds_dwordx4 v[14:15], off
	s_add_i32 s94, s61, s33
	s_mov_b32 s95, 0
	s_cmpk_gt_u32 s94, 0x15ff
	s_cselect_b64 s[96:97], -1, 0
	s_and_b64 s[96:97], s[96:97], exec
	s_cselect_b32 s96, 0x7fffea00, 0
	s_cselect_b32 s98, s25, s15
	s_cselect_b32 s99, s24, s14
	s_add_i32 s96, s96, s94
	s_lshl_b32 s94, s96, 1
	s_addk_i32 s94, 0x2c00
	s_lshl_b64 s[96:97], s[94:95], 12
	s_add_u32 s100, s99, s96
	s_addc_u32 s101, s98, s97
	s_add_i32 s94, s75, s61
	s_cmpk_gt_u32 s94, 0x15ff
	s_cselect_b32 s97, 0x7fffea00, 0
	s_cselect_b32 s96, 0x80, 0
	s_add_i32 s97, s97, s94
	s_lshl_b32 s94, s97, 1
	s_add_i32 s97, s94, 0x2c00
	s_mul_hi_u32 s98, s97, 0xba2e8ba3
	s_lshr_b32 s98, s98, 11
	s_mul_i32 s99, s98, 0x7ffff500
	s_add_i32 s99, s99, s97
	s_lshr_b32 s97, s99, 7
	s_mul_i32 s98, s98, 22
	s_add_i32 s97, s97, s98
	s_lshl_b32 s97, s97, 8
	s_and_b32 s94, s94, 0x7e
	s_or_b32 s96, s97, s96
	s_or_b32 s94, s96, s94
	s_lshl_b64 s[96:97], s[94:95], 11
	s_waitcnt vmcnt(6)
	s_cmp_gt_i32 s61, 44
	s_cbranch_scc1 .Lhka_done_a1
	s_cmp_lt_i32 s61, 1
	s_cbranch_scc1 .Lhka_ld_a1
	v_cvt_pk_f16_f32 v2, v2, v3
	v_cvt_pk_f16_f32 v3, v4, v5
	v_lshl_add_u64 v[4:5], v[224:225], 0, s[96:97]
	global_store_dwordx2 v[4:5], v[2:3], off

.LBB4_40:
	s_add_u32 s28, s46, 0x80
	s_addc_u32 s48, s47, 0
	s_and_b64 s[44:45], s[44:45], exec
	s_cselect_b32 s45, s54, s87
	s_cselect_b32 s44, s55, s86
	s_mov_b32 m0, s59
	v_lshl_add_u64 v[182:183], s[44:45], 0, v[216:217]
	ds_read_b128 v[186:189], v229
	ds_read_b128 v[190:193], v229 offset:1024
	ds_read_b128 v[194:197], v229 offset:2048
	ds_read_b128 v[198:201], v229 offset:3072
	global_load_lds_dwordx4 v[182:183], off
	v_lshl_add_u64 v[184:185], s[44:45], 0, v[218:219]
	s_mov_b32 m0, s60
	s_cselect_b32 s49, s52, s48
	global_load_lds_dwordx4 v[184:185], off
	s_barrier
	s_waitcnt lgkmcnt(0)
	s_cselect_b32 s48, s53, s28
	s_setprio 1
	s_waitcnt lgkmcnt(0)
	v_mfma_f32_16x16x32_f16 v[130:133], v[186:189], v[174:177], v[130:133]
	v_mfma_f32_16x16x32_f16 v[126:129], v[194:197], v[174:177], v[126:129]
	v_mfma_f32_16x16x32_f16 v[122:125], v[186:189], v[166:169], v[122:125]
	v_mfma_f32_16x16x32_f16 v[118:121], v[194:197], v[166:169], v[118:121]
	v_mfma_f32_16x16x32_f16 v[110:113], v[186:189], v[158:161], v[110:113]
	v_mfma_f32_16x16x32_f16 v[102:105], v[194:197], v[158:161], v[102:105]
	v_mfma_f32_16x16x32_f16 v[94:97], v[186:189], v[150:153], v[94:97]
	v_mfma_f32_16x16x32_f16 v[82:85], v[194:197], v[150:153], v[82:85]
	v_mfma_f32_16x16x32_f16 v[130:133], v[190:193], v[178:181], v[130:133]
	v_mfma_f32_16x16x32_f16 v[126:129], v[198:201], v[178:181], v[126:129]
	v_mfma_f32_16x16x32_f16 v[122:125], v[190:193], v[170:173], v[122:125]
	v_mfma_f32_16x16x32_f16 v[118:121], v[198:201], v[170:173], v[118:121]
	v_mfma_f32_16x16x32_f16 v[110:113], v[190:193], v[162:165], v[110:113]
	v_mfma_f32_16x16x32_f16 v[102:105], v[198:201], v[162:165], v[102:105]
	v_mfma_f32_16x16x32_f16 v[94:97], v[190:193], v[154:157], v[94:97]
	v_mfma_f32_16x16x32_f16 v[82:85], v[198:201], v[154:157], v[82:85]
	s_setprio 0
	s_mov_b32 m0, s58
	s_barrier
	ds_read_b128 v[150:153], v237 offset:16384
	ds_read_b128 v[154:157], v237 offset:17408
	ds_read_b128 v[158:161], v237 offset:18432
	ds_read_b128 v[162:165], v237 offset:19456
	ds_read_b128 v[166:169], v237 offset:20480
	ds_read_b128 v[170:173], v237 offset:21504
	ds_read_b128 v[174:177], v237 offset:22528
	ds_read_b128 v[178:181], v237 offset:23552
	global_load_lds_dwordx4 v220, s[48:49]
	s_mov_b32 m0, s62
	s_nop 0
	global_load_lds_dwordx4 v226, s[48:49]
	s_barrier
	s_waitcnt lgkmcnt(0)
	s_setprio 1
	s_waitcnt lgkmcnt(0)
	v_mfma_f32_16x16x32_f16 v[70:73], v[134:137], v[150:153], v[70:73]
	v_mfma_f32_16x16x32_f16 v[58:61], v[142:145], v[150:153], v[58:61]
	v_mfma_f32_16x16x32_f16 v[50:53], v[134:137], v[158:161], v[50:53]
	v_mfma_f32_16x16x32_f16 v[38:41], v[142:145], v[158:161], v[38:41]
	v_mfma_f32_16x16x32_f16 v[26:29], v[134:137], v[166:169], v[26:29]
	v_mfma_f32_16x16x32_f16 v[18:21], v[142:145], v[166:169], v[18:21]
	v_mfma_f32_16x16x32_f16 v[10:13], v[134:137], v[174:177], v[10:13]
	v_mfma_f32_16x16x32_f16 v[6:9], v[142:145], v[174:177], v[6:9]
	v_mfma_f32_16x16x32_f16 v[70:73], v[138:141], v[154:157], v[70:73]
	v_mfma_f32_16x16x32_f16 v[58:61], v[146:149], v[154:157], v[58:61]
	v_mfma_f32_16x16x32_f16 v[50:53], v[138:141], v[162:165], v[50:53]
	v_mfma_f32_16x16x32_f16 v[38:41], v[146:149], v[162:165], v[38:41]
	v_mfma_f32_16x16x32_f16 v[26:29], v[138:141], v[170:173], v[26:29]
	v_mfma_f32_16x16x32_f16 v[18:21], v[146:149], v[170:173], v[18:21]
	v_mfma_f32_16x16x32_f16 v[10:13], v[138:141], v[178:181], v[10:13]
	v_mfma_f32_16x16x32_f16 v[6:9], v[146:149], v[178:181], v[6:9]
	s_setprio 0
	s_barrier
	s_add_u32 s90, s44, 0x40000
	s_addc_u32 s91, s45, 0
	s_mov_b32 m0, s84
	v_lshl_add_u64 v[134:135], s[90:91], 0, v[216:217]
	global_load_lds_dwordx4 v[134:135], off
	v_lshl_add_u64 v[134:135], s[90:91], 0, v[218:219]
	s_mov_b32 m0, s85
	s_nop 0
	global_load_lds_dwordx4 v[134:135], off
	s_add_i32 s94, s61, s33
	s_mov_b32 s95, 0
	s_cmpk_gt_u32 s94, 0x15ff
	s_cselect_b64 s[96:97], -1, 0
	s_and_b64 s[96:97], s[96:97], exec
	s_cselect_b32 s96, 0x7fffea00, 0
	s_cselect_b32 s98, s25, s15
	s_cselect_b32 s99, s24, s14
	s_add_i32 s96, s96, s94
	s_lshl_b32 s94, s96, 1
	s_addk_i32 s94, 0x2c00
	s_lshl_b64 s[96:97], s[94:95], 12
	s_add_u32 s100, s99, s96
	s_addc_u32 s101, s98, s97
	s_add_i32 s94, s75, s61
	s_cmpk_gt_u32 s94, 0x15ff
	s_cselect_b32 s97, 0x7fffea00, 0
	s_cselect_b32 s96, 0x80, 0
	s_add_i32 s97, s97, s94
	s_lshl_b32 s94, s97, 1
	s_add_i32 s97, s94, 0x2c00
	s_mul_hi_u32 s98, s97, 0xba2e8ba3
	s_lshr_b32 s98, s98, 11
	s_mul_i32 s99, s98, 0x7ffff500
	s_add_i32 s99, s99, s97
	s_lshr_b32 s97, s99, 7
	s_mul_i32 s98, s98, 22
	s_add_i32 s97, s97, s98
	s_lshl_b32 s97, s97, 8
	s_and_b32 s94, s94, 0x7e
	s_or_b32 s96, s97, s96
	s_or_b32 s94, s96, s94
	s_lshl_b64 s[96:97], s[94:95], 11
	s_waitcnt vmcnt(6)
	s_cmp_gt_i32 s61, 44
	s_cbranch_scc1 .Lhka_done_a2
	s_cmp_lt_i32 s61, 1
	s_cbranch_scc1 .Lhka_ld_a2
	v_cvt_pk_f16_f32 v2, v2, v3
	v_cvt_pk_f16_f32 v3, v4, v5
	v_lshl_add_u64 v[4:5], v[224:225], 0, s[96:97]
	global_store_dwordx2 v[4:5], v[2:3], off

.LBB4_46:
	s_mov_b32 m0, s67
	v_lshl_add_u64 v[182:183], v[182:183], 0, s[30:31]
	ds_read_b128 v[190:193], v238
	ds_read_b128 v[194:197], v238 offset:1024
	ds_read_b128 v[198:201], v238 offset:2048
	ds_read_b128 v[202:205], v238 offset:3072
	global_load_lds_dwordx4 v[182:183], off
	v_lshl_add_u64 v[182:183], v[184:185], 0, s[30:31]
	s_mov_b32 m0, s68
	v_mov_b32_e32 v227, v221
	global_load_lds_dwordx4 v[182:183], off
	s_barrier
	s_waitcnt lgkmcnt(0)
	v_lshl_add_u64 v[186:187], s[48:49], 0, v[220:221]
	v_lshl_add_u64 v[188:189], s[48:49], 0, v[226:227]
	s_setprio 1
	s_waitcnt lgkmcnt(0)
	v_mfma_f32_16x16x32_f16 v[130:133], v[190:193], v[174:177], v[130:133]
	v_mfma_f32_16x16x32_f16 v[126:129], v[198:201], v[174:177], v[126:129]
	v_mfma_f32_16x16x32_f16 v[122:125], v[190:193], v[166:169], v[122:125]
	v_mfma_f32_16x16x32_f16 v[118:121], v[198:201], v[166:169], v[118:121]
	v_mfma_f32_16x16x32_f16 v[110:113], v[190:193], v[158:161], v[110:113]
	v_mfma_f32_16x16x32_f16 v[102:105], v[198:201], v[158:161], v[102:105]
	v_mfma_f32_16x16x32_f16 v[94:97], v[190:193], v[150:153], v[94:97]
	v_mfma_f32_16x16x32_f16 v[82:85], v[198:201], v[150:153], v[82:85]
	v_mfma_f32_16x16x32_f16 v[130:133], v[194:197], v[178:181], v[130:133]
	v_mfma_f32_16x16x32_f16 v[126:129], v[202:205], v[178:181], v[126:129]
	v_mfma_f32_16x16x32_f16 v[122:125], v[194:197], v[170:173], v[122:125]
	v_mfma_f32_16x16x32_f16 v[118:121], v[202:205], v[170:173], v[118:121]
	v_mfma_f32_16x16x32_f16 v[110:113], v[194:197], v[162:165], v[110:113]
	v_mfma_f32_16x16x32_f16 v[102:105], v[202:205], v[162:165], v[102:105]
	v_mfma_f32_16x16x32_f16 v[94:97], v[194:197], v[154:157], v[94:97]
	v_mfma_f32_16x16x32_f16 v[82:85], v[202:205], v[154:157], v[82:85]
	s_setprio 0
	s_mov_b32 m0, s69
	v_lshl_add_u64 v[182:183], v[186:187], 0, s[30:31]
	s_barrier
	ds_read_b128 v[150:153], v237 offset:49152
	ds_read_b128 v[154:157], v237 offset:50176
	ds_read_b128 v[158:161], v237 offset:51200
	ds_read_b128 v[162:165], v237 offset:52224
	ds_read_b128 v[166:169], v237 offset:53248
	ds_read_b128 v[170:173], v237 offset:54272
	ds_read_b128 v[174:177], v237 offset:55296
	ds_read_b128 v[178:181], v237 offset:56320
	global_load_lds_dwordx4 v[182:183], off
	v_lshl_add_u64 v[182:183], v[188:189], 0, s[30:31]
	s_mov_b32 m0, s70
	s_nop 0
	global_load_lds_dwordx4 v[182:183], off
	s_barrier
	s_waitcnt lgkmcnt(0)
	s_setprio 1
	s_waitcnt lgkmcnt(0)
	v_mfma_f32_16x16x32_f16 v[70:73], v[134:137], v[150:153], v[70:73]
	v_mfma_f32_16x16x32_f16 v[58:61], v[142:145], v[150:153], v[58:61]
	v_mfma_f32_16x16x32_f16 v[50:53], v[134:137], v[158:161], v[50:53]
	v_mfma_f32_16x16x32_f16 v[38:41], v[142:145], v[158:161], v[38:41]
	v_mfma_f32_16x16x32_f16 v[26:29], v[134:137], v[166:169], v[26:29]
	v_mfma_f32_16x16x32_f16 v[18:21], v[142:145], v[166:169], v[18:21]
	v_mfma_f32_16x16x32_f16 v[10:13], v[134:137], v[174:177], v[10:13]
	v_mfma_f32_16x16x32_f16 v[6:9], v[142:145], v[174:177], v[6:9]
	v_mfma_f32_16x16x32_f16 v[70:73], v[138:141], v[154:157], v[70:73]
	v_mfma_f32_16x16x32_f16 v[58:61], v[146:149], v[154:157], v[58:61]
	v_mfma_f32_16x16x32_f16 v[50:53], v[138:141], v[162:165], v[50:53]
	v_mfma_f32_16x16x32_f16 v[38:41], v[146:149], v[162:165], v[38:41]
	v_mfma_f32_16x16x32_f16 v[26:29], v[138:141], v[170:173], v[26:29]
	v_mfma_f32_16x16x32_f16 v[18:21], v[146:149], v[170:173], v[18:21]
	v_mfma_f32_16x16x32_f16 v[10:13], v[138:141], v[178:181], v[10:13]
	v_mfma_f32_16x16x32_f16 v[6:9], v[146:149], v[178:181], v[6:9]
	s_setprio 0
	s_barrier
	s_add_u32 s44, s44, 0x40080
	s_addc_u32 s45, s45, 0
	s_mov_b32 m0, s50
	v_lshl_add_u64 v[134:135], s[44:45], 0, v[216:217]
	global_load_lds_dwordx4 v[134:135], off
	v_lshl_add_u64 v[134:135], s[44:45], 0, v[218:219]
	s_mov_b32 m0, s51
	s_nop 0
	global_load_lds_dwordx4 v[134:135], off
	s_add_i32 s94, s61, s33
	s_mov_b32 s95, 0
	s_cmpk_gt_u32 s94, 0x15ff
	s_cselect_b64 s[96:97], -1, 0
	s_and_b64 s[96:97], s[96:97], exec
	s_cselect_b32 s96, 0x7fffea00, 0
	s_cselect_b32 s98, s25, s15
	s_cselect_b32 s99, s24, s14
	s_add_i32 s96, s96, s94
	s_lshl_b32 s94, s96, 1
	s_addk_i32 s94, 0x2c00
	s_lshl_b64 s[96:97], s[94:95], 12
	s_add_u32 s100, s99, s96
	s_addc_u32 s101, s98, s97
	s_add_i32 s94, s75, s61
	s_cmpk_gt_u32 s94, 0x15ff
	s_cselect_b32 s97, 0x7fffea00, 0
	s_cselect_b32 s96, 0x80, 0
	s_add_i32 s97, s97, s94
	s_lshl_b32 s94, s97, 1
	s_add_i32 s97, s94, 0x2c00
	s_mul_hi_u32 s98, s97, 0xba2e8ba3
	s_lshr_b32 s98, s98, 11
	s_mul_i32 s99, s98, 0x7ffff500
	s_add_i32 s99, s99, s97
	s_lshr_b32 s97, s99, 7
	s_mul_i32 s98, s98, 22
	s_add_i32 s97, s97, s98
	s_lshl_b32 s97, s97, 8
	s_and_b32 s94, s94, 0x7e
	s_or_b32 s96, s97, s96
	s_or_b32 s94, s96, s94
	s_lshl_b64 s[96:97], s[94:95], 11
	s_waitcnt vmcnt(6)
	s_cmp_gt_i32 s61, 44
	s_cbranch_scc1 .Lhka_done_a3
	s_cmp_lt_i32 s61, 1
	s_cbranch_scc1 .Lhka_ld_a3
	v_cvt_pk_f16_f32 v2, v2, v3
	v_cvt_pk_f16_f32 v3, v4, v5
	v_lshl_add_u64 v[4:5], v[224:225], 0, s[96:97]
	global_store_dwordx2 v[4:5], v[2:3], off

	.amdhsa_kernel _Z7k_gemm1ILi0EEvPKDF16_S1_PDF16_PK15HIP_vector_typeIiLj2EEPKfS8_S2_PKt
		.amdhsa_group_segment_fixed_size 0
		.amdhsa_private_segment_fixed_size 0
		.amdhsa_kernarg_size 64
		.amdhsa_user_sgpr_count 2
		.amdhsa_user_sgpr_dispatch_ptr 0
		.amdhsa_user_sgpr_queue_ptr 0
		.amdhsa_user_sgpr_kernarg_segment_ptr 1
		.amdhsa_user_sgpr_dispatch_id 0
		.amdhsa_user_sgpr_kernarg_preload_length 0
		.amdhsa_user_sgpr_kernarg_preload_offset 0
		.amdhsa_user_sgpr_private_segment_size 0
		.amdhsa_uses_dynamic_stack 0
		.amdhsa_enable_private_segment 0
		.amdhsa_system_sgpr_workgroup_id_x 1
		.amdhsa_system_sgpr_workgroup_id_y 0
		.amdhsa_system_sgpr_workgroup_id_z 0
		.amdhsa_system_sgpr_workgroup_info 0
		.amdhsa_system_vgpr_workitem_id 0
		.amdhsa_next_free_vgpr 256
		.amdhsa_next_free_sgpr 102
		.amdhsa_accum_offset 256
		.amdhsa_reserve_vcc 1
		.amdhsa_float_round_mode_32 0
		.amdhsa_float_round_mode_16_64 0
		.amdhsa_float_denorm_mode_32 3
		.amdhsa_float_denorm_mode_16_64 3
		.amdhsa_dx10_clamp 1
		.amdhsa_ieee_mode 1
		.amdhsa_fp16_overflow 0
		.amdhsa_tg_split 0
		.amdhsa_exception_fp_ieee_invalid_op 0
		.amdhsa_exception_fp_denorm_src 0
		.amdhsa_exception_fp_ieee_div_zero 0
		.amdhsa_exception_fp_ieee_overflow 0
		.amdhsa_exception_fp_ieee_underflow 0
		.amdhsa_exception_fp_ieee_inexact 0
		.amdhsa_exception_int_div_zero 0
	.end_amdhsa_kernel

.LBB5_18:
.LBB5_24:
	s_and_b64 s[46:47], s[38:39], exec
	s_cselect_b32 s48, s35, s43
	s_cselect_b32 s49, s34, s42
	s_cselect_b32 s50, s37, s41
	s_cselect_b32 s51, s36, s40
	s_add_u32 s24, s42, 0x100
	s_addc_u32 s80, s43, 0
	s_and_b64 s[46:47], s[44:45], exec
	s_cselect_b32 s47, s48, s80
	s_cselect_b32 s46, s49, s24
	s_add_u32 s24, s40, 0x100
	s_addc_u32 s80, s41, 0
	s_and_b64 s[44:45], s[44:45], exec
	s_cselect_b32 s45, s50, s80
	s_cselect_b32 s44, s51, s24
	s_mov_b32 m0, s55
	v_add_u32_e32 v227, s72, v232
	v_lshl_add_u64 v[130:131], s[44:45], 0, v[212:213]
	ds_read_b128 v[82:85], v227
	ds_read_b128 v[94:97], v227 offset:1024
	ds_read_b128 v[102:105], v227 offset:2048
	ds_read_b128 v[110:113], v227 offset:3072
	global_load_lds_dwordx4 v[130:131], off
	v_lshl_add_u64 v[132:133], s[44:45], 0, v[214:215]
	s_mov_b32 m0, s56
	s_nop 0
	global_load_lds_dwordx4 v[132:133], off
	s_barrier
	s_waitcnt lgkmcnt(0)
	s_setprio 1
	s_waitcnt lgkmcnt(0)
	v_mfma_f32_16x16x32_f16 v[90:93], v[82:85], v[46:49], 0
	v_mfma_f32_16x16x32_f16 v[46:49], v[102:105], v[46:49], 0
	v_mfma_f32_16x16x32_f16 v[90:93], v[94:97], v[50:53], v[90:93]
	v_mfma_f32_16x16x32_f16 v[46:49], v[110:113], v[50:53], v[46:49]
	v_mfma_f32_16x16x32_f16 v[50:53], v[82:85], v[38:41], 0
	v_mfma_f32_16x16x32_f16 v[38:41], v[102:105], v[38:41], 0
	v_mfma_f32_16x16x32_f16 v[106:109], v[110:113], v[42:45], v[38:41]
	v_mfma_f32_16x16x32_f16 v[38:41], v[82:85], v[30:33], 0
	v_mfma_f32_16x16x32_f16 v[30:33], v[102:105], v[30:33], 0
	v_mfma_f32_16x16x32_f16 v[170:173], v[110:113], v[34:37], v[30:33]
	v_mfma_f32_16x16x32_f16 v[30:33], v[82:85], v[22:25], 0
	v_mfma_f32_16x16x32_f16 v[22:25], v[102:105], v[22:25], 0
	v_mfma_f32_16x16x32_f16 v[98:101], v[94:97], v[42:45], v[50:53]
	v_mfma_f32_16x16x32_f16 v[166:169], v[94:97], v[34:37], v[38:41]
	v_mfma_f32_16x16x32_f16 v[174:177], v[94:97], v[26:29], v[30:33]
	v_mfma_f32_16x16x32_f16 v[178:181], v[110:113], v[26:29], v[22:25]
	s_setprio 0
	s_mov_b32 m0, s54
	s_barrier
	ds_read_b128 v[42:45], v235 offset:16384
	ds_read_b128 v[114:117], v235 offset:17408
	ds_read_b128 v[118:121], v235 offset:18432
	ds_read_b128 v[122:125], v235 offset:19456
	ds_read_b128 v[126:129], v235 offset:20480
	ds_read_b128 v[154:157], v235 offset:21504
	ds_read_b128 v[162:165], v235 offset:22528
	ds_read_b128 v[182:185], v235 offset:23552
	global_load_lds_dwordx4 v216, s[46:47]
	s_mov_b32 m0, s57
	s_nop 0
	global_load_lds_dwordx4 v222, s[46:47]
	s_barrier
	s_waitcnt lgkmcnt(0)
	s_setprio 1
	s_waitcnt lgkmcnt(0)
	v_mfma_f32_16x16x32_f16 v[22:25], v[6:9], v[42:45], 0
	v_mfma_f32_16x16x32_f16 v[30:33], v[6:9], v[118:121], 0
	v_mfma_f32_16x16x32_f16 v[38:41], v[6:9], v[126:129], 0
	v_mfma_f32_16x16x32_f16 v[6:9], v[6:9], v[162:165], 0
	v_mfma_f32_16x16x32_f16 v[22:25], v[10:13], v[114:117], v[22:25]
	v_mfma_f32_16x16x32_f16 v[26:29], v[14:17], v[42:45], 0
	v_mfma_f32_16x16x32_f16 v[30:33], v[10:13], v[122:125], v[30:33]
	v_mfma_f32_16x16x32_f16 v[34:37], v[14:17], v[118:121], 0
	v_mfma_f32_16x16x32_f16 v[38:41], v[10:13], v[154:157], v[38:41]
	v_mfma_f32_16x16x32_f16 v[50:53], v[14:17], v[126:129], 0
	v_mfma_f32_16x16x32_f16 v[6:9], v[10:13], v[182:185], v[6:9]
	v_mfma_f32_16x16x32_f16 v[10:13], v[14:17], v[162:165], 0
	v_mfma_f32_16x16x32_f16 v[26:29], v[18:21], v[114:117], v[26:29]
	v_mfma_f32_16x16x32_f16 v[34:37], v[18:21], v[122:125], v[34:37]
	v_mfma_f32_16x16x32_f16 v[50:53], v[18:21], v[154:157], v[50:53]
	v_mfma_f32_16x16x32_f16 v[14:17], v[18:21], v[182:185], v[10:13]
	s_setprio 0
	s_barrier
	s_add_u32 s82, s44, 0x40000
	s_addc_u32 s83, s45, 0
	s_add_i32 s80, s72, s53
	v_lshl_add_u64 v[10:11], s[82:83], 0, v[212:213]
	s_mov_b32 m0, s80
	s_add_i32 s81, s80, 0x2000
	global_load_lds_dwordx4 v[10:11], off
	v_lshl_add_u64 v[10:11], s[82:83], 0, v[214:215]
	s_mov_b32 m0, s81
	s_nop 0
	global_load_lds_dwordx4 v[10:11], off
	s_add_i32 s92, s71, s63
	s_mov_b32 s93, 0
	s_lshl_b64 s[90:91], s[92:93], 12
	s_add_i32 s92, s63, s33
	s_lshl_b64 s[92:93], s[92:93], 13
	s_waitcnt vmcnt(6)
	s_cmp_gt_i32 s63, 44
	s_cbranch_scc1 .Lhkb_done_b0
	s_cmp_lt_i32 s63, 1
	s_cbranch_scc1 .Lhkb_ld_b0
	v_cvt_pk_f16_f32 v2, v2, v3
	v_cvt_pk_f16_f32 v3, v4, v5
	v_lshl_add_u64 v[4:5], v[220:221], 0, s[90:91]
	global_store_dwordx2 v[4:5], v[2:3], off
.Lhkb_ld_b0:
	s_cmp_eq_u32 s63, 44
	s_cbranch_scc1 .Lhkb_inc_b0
	v_lshl_add_u64 v[4:5], v[224:225], 0, s[92:93]
	global_load_dwordx4 v[2:5], v[4:5], off nt

.LBB5_30:
	v_mov_b32_e32 v223, v217
	v_lshl_add_u64 v[58:59], s[46:47], 0, v[216:217]
	v_lshl_add_u64 v[60:61], s[46:47], 0, v[222:223]
	s_add_i32 s46, 0, 0x1c000
	s_mov_b32 m0, s62
	v_add_u32_e32 v236, s46, v232
	v_lshl_add_u64 v[62:63], v[130:131], 0, s[26:27]
	ds_read_b128 v[238:241], v236
	ds_read_b128 v[242:245], v236 offset:1024
	ds_read_b128 v[246:249], v236 offset:2048
	ds_read_b128 v[250:253], v236 offset:3072
	global_load_lds_dwordx4 v[62:63], off
	v_lshl_add_u64 v[62:63], v[132:133], 0, s[26:27]
	s_mov_b32 m0, s64
	s_nop 0
	global_load_lds_dwordx4 v[62:63], off
	s_barrier
	s_waitcnt lgkmcnt(0)
	s_setprio 1
	s_waitcnt lgkmcnt(0)
	v_mfma_f32_16x16x32_f16 v[62:65], v[238:241], v[122:125], v[90:93]
	v_mfma_f32_16x16x32_f16 v[46:49], v[246:249], v[122:125], v[46:49]
	v_mfma_f32_16x16x32_f16 v[130:133], v[242:245], v[126:129], v[62:65]
	v_mfma_f32_16x16x32_f16 v[126:129], v[250:253], v[126:129], v[46:49]
	v_mfma_f32_16x16x32_f16 v[46:49], v[238:241], v[114:117], v[98:101]
	v_mfma_f32_16x16x32_f16 v[122:125], v[242:245], v[206:209], v[46:49]
	v_mfma_f32_16x16x32_f16 v[46:49], v[246:249], v[114:117], v[106:109]
	v_mfma_f32_16x16x32_f16 v[114:117], v[250:253], v[206:209], v[46:49]
	v_mfma_f32_16x16x32_f16 v[46:49], v[238:241], v[198:201], v[166:169]
	v_mfma_f32_16x16x32_f16 v[106:109], v[242:245], v[202:205], v[46:49]
	v_mfma_f32_16x16x32_f16 v[46:49], v[246:249], v[198:201], v[170:173]
	v_mfma_f32_16x16x32_f16 v[98:101], v[250:253], v[202:205], v[46:49]
	v_mfma_f32_16x16x32_f16 v[46:49], v[238:241], v[18:21], v[174:177]
	v_mfma_f32_16x16x32_f16 v[18:21], v[246:249], v[18:21], v[178:181]
	v_mfma_f32_16x16x32_f16 v[90:93], v[242:245], v[194:197], v[46:49]
	v_mfma_f32_16x16x32_f16 v[78:81], v[250:253], v[194:197], v[18:21]
	s_setprio 0
	s_mov_b32 m0, s65
	s_nop 3
	v_lshl_add_u64 v[18:19], v[58:59], 0, s[26:27]
	s_barrier
	ds_read_b128 v[62:65], v235 offset:49152
	ds_read_b128 v[74:77], v235 offset:50176
	ds_read_b128 v[166:169], v235 offset:51200
	ds_read_b128 v[170:173], v235 offset:52224
	ds_read_b128 v[174:177], v235 offset:53248
	ds_read_b128 v[178:181], v235 offset:54272
	ds_read_b128 v[194:197], v235 offset:55296
	ds_read_b128 v[198:201], v235 offset:56320
	global_load_lds_dwordx4 v[18:19], off
	v_lshl_add_u64 v[18:19], v[60:61], 0, s[26:27]
	s_mov_b32 m0, s66
	s_nop 0
	global_load_lds_dwordx4 v[18:19], off
	s_barrier
	s_waitcnt lgkmcnt(0)
	s_setprio 1
	s_waitcnt lgkmcnt(0)
	v_mfma_f32_16x16x32_f16 v[18:21], v[10:13], v[62:65], v[22:25]
	v_mfma_f32_16x16x32_f16 v[70:73], v[182:185], v[74:77], v[18:21]
	v_mfma_f32_16x16x32_f16 v[18:21], v[186:189], v[62:65], v[26:29]
	v_mfma_f32_16x16x32_f16 v[58:61], v[190:193], v[74:77], v[18:21]
	v_mfma_f32_16x16x32_f16 v[18:21], v[10:13], v[166:169], v[30:33]
	v_mfma_f32_16x16x32_f16 v[46:49], v[182:185], v[170:173], v[18:21]
	v_mfma_f32_16x16x32_f16 v[18:21], v[186:189], v[166:169], v[34:37]
	v_mfma_f32_16x16x32_f16 v[34:37], v[190:193], v[170:173], v[18:21]
	v_mfma_f32_16x16x32_f16 v[18:21], v[10:13], v[174:177], v[38:41]
	v_mfma_f32_16x16x32_f16 v[6:9], v[10:13], v[194:197], v[6:9]
	v_mfma_f32_16x16x32_f16 v[26:29], v[182:185], v[178:181], v[18:21]
	v_mfma_f32_16x16x32_f16 v[18:21], v[186:189], v[174:177], v[50:53]
	v_mfma_f32_16x16x32_f16 v[10:13], v[182:185], v[198:201], v[6:9]
	v_mfma_f32_16x16x32_f16 v[6:9], v[186:189], v[194:197], v[14:17]
	v_mfma_f32_16x16x32_f16 v[18:21], v[190:193], v[178:181], v[18:21]
	v_mfma_f32_16x16x32_f16 v[6:9], v[190:193], v[198:201], v[6:9]
	s_setprio 0
	s_barrier
	s_add_u32 s44, s44, 0x40080
	s_addc_u32 s45, s45, 0
	s_add_i32 s46, s46, s53
	v_lshl_add_u64 v[14:15], s[44:45], 0, v[212:213]
	s_mov_b32 m0, s46
	s_add_i32 s47, s46, 0x2000
	global_load_lds_dwordx4 v[14:15], off
	v_lshl_add_u64 v[14:15], s[44:45], 0, v[214:215]
	s_mov_b32 m0, s47
	s_nop 0
	global_load_lds_dwordx4 v[14:15], off
	s_add_i32 s92, s71, s63
	s_mov_b32 s93, 0
	s_lshl_b64 s[90:91], s[92:93], 12
	s_add_i32 s92, s63, s33
	s_lshl_b64 s[92:93], s[92:93], 13
	s_waitcnt vmcnt(6)
	s_cmp_gt_i32 s63, 44
	s_cbranch_scc1 .Lhkb_done_b1
	s_cmp_lt_i32 s63, 1
	s_cbranch_scc1 .Lhkb_ld_b1
	v_cvt_pk_f16_f32 v2, v2, v3
	v_cvt_pk_f16_f32 v3, v4, v5
	v_lshl_add_u64 v[4:5], v[220:221], 0, s[90:91]
	global_store_dwordx2 v[4:5], v[2:3], off

.LBB5_40:
	s_add_u32 s24, s42, 0x80
	s_addc_u32 s44, s43, 0
	s_and_b64 s[40:41], s[40:41], exec
	s_cselect_b32 s41, s50, s83
	s_cselect_b32 s40, s51, s82
	s_mov_b32 m0, s55
	v_lshl_add_u64 v[182:183], s[40:41], 0, v[212:213]
	ds_read_b128 v[186:189], v227
	ds_read_b128 v[190:193], v227 offset:1024
	ds_read_b128 v[194:197], v227 offset:2048
	ds_read_b128 v[198:201], v227 offset:3072
	global_load_lds_dwordx4 v[182:183], off
	v_lshl_add_u64 v[184:185], s[40:41], 0, v[214:215]
	s_mov_b32 m0, s56
	s_cselect_b32 s45, s48, s44
	global_load_lds_dwordx4 v[184:185], off
	s_barrier
	s_waitcnt lgkmcnt(0)
	s_cselect_b32 s44, s49, s24
	s_setprio 1
	s_waitcnt lgkmcnt(0)
	v_mfma_f32_16x16x32_f16 v[130:133], v[186:189], v[174:177], v[130:133]
	v_mfma_f32_16x16x32_f16 v[126:129], v[194:197], v[174:177], v[126:129]
	v_mfma_f32_16x16x32_f16 v[122:125], v[186:189], v[166:169], v[122:125]
	v_mfma_f32_16x16x32_f16 v[114:117], v[194:197], v[166:169], v[114:117]
	v_mfma_f32_16x16x32_f16 v[106:109], v[186:189], v[158:161], v[106:109]
	v_mfma_f32_16x16x32_f16 v[98:101], v[194:197], v[158:161], v[98:101]
	v_mfma_f32_16x16x32_f16 v[90:93], v[186:189], v[150:153], v[90:93]
	v_mfma_f32_16x16x32_f16 v[78:81], v[194:197], v[150:153], v[78:81]
	v_mfma_f32_16x16x32_f16 v[130:133], v[190:193], v[178:181], v[130:133]
	v_mfma_f32_16x16x32_f16 v[126:129], v[198:201], v[178:181], v[126:129]
	v_mfma_f32_16x16x32_f16 v[122:125], v[190:193], v[170:173], v[122:125]
	v_mfma_f32_16x16x32_f16 v[114:117], v[198:201], v[170:173], v[114:117]
	v_mfma_f32_16x16x32_f16 v[106:109], v[190:193], v[162:165], v[106:109]
	v_mfma_f32_16x16x32_f16 v[98:101], v[198:201], v[162:165], v[98:101]
	v_mfma_f32_16x16x32_f16 v[90:93], v[190:193], v[154:157], v[90:93]
	v_mfma_f32_16x16x32_f16 v[78:81], v[198:201], v[154:157], v[78:81]
	s_setprio 0
	s_mov_b32 m0, s54
	s_barrier
	ds_read_b128 v[150:153], v235 offset:16384
	ds_read_b128 v[154:157], v235 offset:17408
	ds_read_b128 v[158:161], v235 offset:18432
	ds_read_b128 v[162:165], v235 offset:19456
	ds_read_b128 v[166:169], v235 offset:20480
	ds_read_b128 v[170:173], v235 offset:21504
	ds_read_b128 v[174:177], v235 offset:22528
	ds_read_b128 v[178:181], v235 offset:23552
	global_load_lds_dwordx4 v216, s[44:45]
	s_mov_b32 m0, s57
	s_nop 0
	global_load_lds_dwordx4 v222, s[44:45]
	s_barrier
	s_waitcnt lgkmcnt(0)
	s_setprio 1
	s_waitcnt lgkmcnt(0)
	v_mfma_f32_16x16x32_f16 v[70:73], v[134:137], v[150:153], v[70:73]
	v_mfma_f32_16x16x32_f16 v[58:61], v[142:145], v[150:153], v[58:61]
	v_mfma_f32_16x16x32_f16 v[46:49], v[134:137], v[158:161], v[46:49]
	v_mfma_f32_16x16x32_f16 v[34:37], v[142:145], v[158:161], v[34:37]
	v_mfma_f32_16x16x32_f16 v[26:29], v[134:137], v[166:169], v[26:29]
	v_mfma_f32_16x16x32_f16 v[18:21], v[142:145], v[166:169], v[18:21]
	v_mfma_f32_16x16x32_f16 v[10:13], v[134:137], v[174:177], v[10:13]
	v_mfma_f32_16x16x32_f16 v[6:9], v[142:145], v[174:177], v[6:9]
	v_mfma_f32_16x16x32_f16 v[70:73], v[138:141], v[154:157], v[70:73]
	v_mfma_f32_16x16x32_f16 v[58:61], v[146:149], v[154:157], v[58:61]
	v_mfma_f32_16x16x32_f16 v[46:49], v[138:141], v[162:165], v[46:49]
	v_mfma_f32_16x16x32_f16 v[34:37], v[146:149], v[162:165], v[34:37]
	v_mfma_f32_16x16x32_f16 v[26:29], v[138:141], v[170:173], v[26:29]
	v_mfma_f32_16x16x32_f16 v[18:21], v[146:149], v[170:173], v[18:21]
	v_mfma_f32_16x16x32_f16 v[10:13], v[138:141], v[178:181], v[10:13]
	v_mfma_f32_16x16x32_f16 v[6:9], v[146:149], v[178:181], v[6:9]
	s_setprio 0
	s_barrier
	s_add_u32 s86, s40, 0x40000
	s_addc_u32 s87, s41, 0
	s_mov_b32 m0, s80
	v_lshl_add_u64 v[134:135], s[86:87], 0, v[212:213]
	global_load_lds_dwordx4 v[134:135], off
	v_lshl_add_u64 v[134:135], s[86:87], 0, v[214:215]
	s_mov_b32 m0, s81
	s_nop 0
	global_load_lds_dwordx4 v[134:135], off
	s_add_i32 s92, s71, s63
	s_mov_b32 s93, 0
	s_lshl_b64 s[90:91], s[92:93], 12
	s_add_i32 s92, s63, s33
	s_lshl_b64 s[92:93], s[92:93], 13
	s_waitcnt vmcnt(6)
	s_cmp_gt_i32 s63, 44
	s_cbranch_scc1 .Lhkb_done_b2
	s_cmp_lt_i32 s63, 1
	s_cbranch_scc1 .Lhkb_ld_b2
	v_cvt_pk_f16_f32 v2, v2, v3
	v_cvt_pk_f16_f32 v3, v4, v5
	v_lshl_add_u64 v[4:5], v[220:221], 0, s[90:91]
	global_store_dwordx2 v[4:5], v[2:3], off

.LBB5_46:
	s_mov_b32 m0, s62
	v_lshl_add_u64 v[182:183], v[182:183], 0, s[26:27]
	ds_read_b128 v[190:193], v236
	ds_read_b128 v[194:197], v236 offset:1024
	ds_read_b128 v[198:201], v236 offset:2048
	ds_read_b128 v[202:205], v236 offset:3072
	global_load_lds_dwordx4 v[182:183], off
	v_lshl_add_u64 v[182:183], v[184:185], 0, s[26:27]
	s_mov_b32 m0, s64
	v_mov_b32_e32 v223, v217
	global_load_lds_dwordx4 v[182:183], off
	s_barrier
	s_waitcnt lgkmcnt(0)
	v_lshl_add_u64 v[186:187], s[44:45], 0, v[216:217]
	v_lshl_add_u64 v[188:189], s[44:45], 0, v[222:223]
	s_setprio 1
	s_waitcnt lgkmcnt(0)
	v_mfma_f32_16x16x32_f16 v[130:133], v[190:193], v[174:177], v[130:133]
	v_mfma_f32_16x16x32_f16 v[126:129], v[198:201], v[174:177], v[126:129]
	v_mfma_f32_16x16x32_f16 v[122:125], v[190:193], v[166:169], v[122:125]
	v_mfma_f32_16x16x32_f16 v[114:117], v[198:201], v[166:169], v[114:117]
	v_mfma_f32_16x16x32_f16 v[106:109], v[190:193], v[158:161], v[106:109]
	v_mfma_f32_16x16x32_f16 v[98:101], v[198:201], v[158:161], v[98:101]
	v_mfma_f32_16x16x32_f16 v[90:93], v[190:193], v[150:153], v[90:93]
	v_mfma_f32_16x16x32_f16 v[78:81], v[198:201], v[150:153], v[78:81]
	v_mfma_f32_16x16x32_f16 v[130:133], v[194:197], v[178:181], v[130:133]
	v_mfma_f32_16x16x32_f16 v[126:129], v[202:205], v[178:181], v[126:129]
	v_mfma_f32_16x16x32_f16 v[122:125], v[194:197], v[170:173], v[122:125]
	v_mfma_f32_16x16x32_f16 v[114:117], v[202:205], v[170:173], v[114:117]
	v_mfma_f32_16x16x32_f16 v[106:109], v[194:197], v[162:165], v[106:109]
	v_mfma_f32_16x16x32_f16 v[98:101], v[202:205], v[162:165], v[98:101]
	v_mfma_f32_16x16x32_f16 v[90:93], v[194:197], v[154:157], v[90:93]
	v_mfma_f32_16x16x32_f16 v[78:81], v[202:205], v[154:157], v[78:81]
	s_setprio 0
	s_mov_b32 m0, s65
	v_lshl_add_u64 v[182:183], v[186:187], 0, s[26:27]
	s_barrier
	ds_read_b128 v[150:153], v235 offset:49152
	ds_read_b128 v[154:157], v235 offset:50176
	ds_read_b128 v[158:161], v235 offset:51200
	ds_read_b128 v[162:165], v235 offset:52224
	ds_read_b128 v[166:169], v235 offset:53248
	ds_read_b128 v[170:173], v235 offset:54272
	ds_read_b128 v[174:177], v235 offset:55296
	ds_read_b128 v[178:181], v235 offset:56320
	global_load_lds_dwordx4 v[182:183], off
	v_lshl_add_u64 v[182:183], v[188:189], 0, s[26:27]
	s_mov_b32 m0, s66
	s_nop 0
	global_load_lds_dwordx4 v[182:183], off
	s_barrier
	s_waitcnt lgkmcnt(0)
	s_setprio 1
	s_waitcnt lgkmcnt(0)
	v_mfma_f32_16x16x32_f16 v[70:73], v[134:137], v[150:153], v[70:73]
	v_mfma_f32_16x16x32_f16 v[58:61], v[142:145], v[150:153], v[58:61]
	v_mfma_f32_16x16x32_f16 v[46:49], v[134:137], v[158:161], v[46:49]
	v_mfma_f32_16x16x32_f16 v[34:37], v[142:145], v[158:161], v[34:37]
	v_mfma_f32_16x16x32_f16 v[26:29], v[134:137], v[166:169], v[26:29]
	v_mfma_f32_16x16x32_f16 v[18:21], v[142:145], v[166:169], v[18:21]
	v_mfma_f32_16x16x32_f16 v[10:13], v[134:137], v[174:177], v[10:13]
	v_mfma_f32_16x16x32_f16 v[6:9], v[142:145], v[174:177], v[6:9]
	v_mfma_f32_16x16x32_f16 v[70:73], v[138:141], v[154:157], v[70:73]
	v_mfma_f32_16x16x32_f16 v[58:61], v[146:149], v[154:157], v[58:61]
	v_mfma_f32_16x16x32_f16 v[46:49], v[138:141], v[162:165], v[46:49]
	v_mfma_f32_16x16x32_f16 v[34:37], v[146:149], v[162:165], v[34:37]
	v_mfma_f32_16x16x32_f16 v[26:29], v[138:141], v[170:173], v[26:29]
	v_mfma_f32_16x16x32_f16 v[18:21], v[146:149], v[170:173], v[18:21]
	v_mfma_f32_16x16x32_f16 v[10:13], v[138:141], v[178:181], v[10:13]
	v_mfma_f32_16x16x32_f16 v[6:9], v[146:149], v[178:181], v[6:9]
	s_setprio 0
	s_barrier
	s_add_u32 s40, s40, 0x40080
	s_addc_u32 s41, s41, 0
	s_mov_b32 m0, s46
	v_lshl_add_u64 v[134:135], s[40:41], 0, v[212:213]
	global_load_lds_dwordx4 v[134:135], off
	v_lshl_add_u64 v[134:135], s[40:41], 0, v[214:215]
	s_mov_b32 m0, s47
	s_nop 0
	global_load_lds_dwordx4 v[134:135], off
	s_add_i32 s92, s71, s63
	s_mov_b32 s93, 0
	s_lshl_b64 s[90:91], s[92:93], 12
	s_add_i32 s92, s63, s33
	s_lshl_b64 s[92:93], s[92:93], 13
	s_waitcnt vmcnt(6)
	s_cmp_gt_i32 s63, 44
	s_cbranch_scc1 .Lhkb_done_b3
	s_cmp_lt_i32 s63, 1
	s_cbranch_scc1 .Lhkb_ld_b3
	v_cvt_pk_f16_f32 v2, v2, v3
	v_cvt_pk_f16_f32 v3, v4, v5
	v_lshl_add_u64 v[4:5], v[220:221], 0, s[90:91]
	global_store_dwordx2 v[4:5], v[2:3], off

amdhsa.kernels:
  - .agpr_count:     0
    .args:
      - .actual_access:  read_only
        .address_space:  global
        .offset:         0
        .size:           8
        .value_kind:     global_buffer
      - .actual_access:  read_only
        .address_space:  global
        .offset:         8
        .size:           8
        .value_kind:     global_buffer
      - .actual_access:  write_only
        .address_space:  global
        .offset:         16
        .size:           8
        .value_kind:     global_buffer
      - .actual_access:  write_only
        .address_space:  global
        .offset:         24
        .size:           8
        .value_kind:     global_buffer
      - .actual_access:  write_only
        .address_space:  global
        .offset:         32
        .size:           8
        .value_kind:     global_buffer
      - .actual_access:  write_only
        .address_space:  global
        .offset:         40
        .size:           8
        .value_kind:     global_buffer
    .group_segment_fixed_size: 256
    .kernarg_segment_align: 8
    .kernarg_segment_size: 48
    .language:       OpenCL C
    .language_version:
      - 2
      - 0
    .max_flat_workgroup_size: 256
    .name:           _Z10k_xscatterPKiS0_P15HIP_vector_typeIiLj2EEPtP4MetaS3_
    .private_segment_fixed_size: 0
    .sgpr_count:     41
    .sgpr_spill_count: 0
    .symbol:         _Z10k_xscatterPKiS0_P15HIP_vector_typeIiLj2EEPtP4MetaS3_.kd
    .uniform_work_group_size: 1
    .uses_dynamic_stack: false
    .vgpr_count:     55
    .vgpr_spill_count: 0
    .wavefront_size: 64
  - .agpr_count:     0
    .args:
      - .actual_access:  read_only
        .address_space:  global
        .offset:         0
        .size:           8
        .value_kind:     global_buffer
      - .actual_access:  read_only
        .address_space:  global
        .offset:         8
        .size:           8
        .value_kind:     global_buffer
      - .actual_access:  write_only
        .address_space:  global
        .offset:         16
        .size:           8
        .value_kind:     global_buffer
      - .actual_access:  write_only
        .address_space:  global
        .offset:         24
        .size:           8
        .value_kind:     global_buffer
      - .actual_access:  write_only
        .address_space:  global
        .offset:         32
        .size:           8
        .value_kind:     global_buffer
      - .actual_access:  read_only
        .address_space:  global
        .offset:         40
        .size:           8
        .value_kind:     global_buffer
      - .actual_access:  read_only
        .address_space:  global
        .offset:         48
        .size:           8
        .value_kind:     global_buffer
      - .actual_access:  write_only
        .address_space:  global
        .offset:         56
        .size:           8
        .value_kind:     global_buffer
      - .actual_access:  write_only
        .address_space:  global
        .offset:         64
        .size:           8
        .value_kind:     global_buffer
    .group_segment_fixed_size: 4096
    .kernarg_segment_align: 8
    .kernarg_segment_size: 72
    .language:       OpenCL C
    .language_version:
      - 2
      - 0
    .max_flat_workgroup_size: 256
    .name:           _Z5k_prePKfS0_PiP15HIP_vector_typeIfLj2EES1_S0_S0_PDF16_S5_
    .private_segment_fixed_size: 0
    .sgpr_count:     42
    .sgpr_spill_count: 0
    .symbol:         _Z5k_prePKfS0_PiP15HIP_vector_typeIfLj2EES1_S0_S0_PDF16_S5_.kd
    .uniform_work_group_size: 1
    .uses_dynamic_stack: false
    .vgpr_count:     128
    .vgpr_spill_count: 0
    .wavefront_size: 64
  - .agpr_count:     0
    .args:
      - .address_space:  global
        .offset:         0
        .size:           8
        .value_kind:     global_buffer
      - .address_space:  global
        .offset:         8
        .size:           8
        .value_kind:     global_buffer
      - .actual_access:  write_only
        .address_space:  global
        .offset:         16
        .size:           8
        .value_kind:     global_buffer
      - .actual_access:  read_only
        .address_space:  global
        .offset:         24
        .size:           8
        .value_kind:     global_buffer
    .group_segment_fixed_size: 0
    .kernarg_segment_align: 8
    .kernarg_segment_size: 32
    .language:       OpenCL C
    .language_version:
      - 2
      - 0
    .max_flat_workgroup_size: 512
    .name:           _Z7k_gemm2PKDF16_S0_PDF16_PK15HIP_vector_typeIiLj2EE
    .private_segment_fixed_size: 0
    .sgpr_count:     74
    .sgpr_spill_count: 0
    .symbol:         _Z7k_gemm2PKDF16_S0_PDF16_PK15HIP_vector_typeIiLj2EE.kd
    .uniform_work_group_size: 1
    .uses_dynamic_stack: false
    .vgpr_count:     226
    .vgpr_spill_count: 0
    .wavefront_size: 64
  - .agpr_count:     0
    .args:
      - .actual_access:  read_only
        .address_space:  global
        .offset:         0
        .size:           8
        .value_kind:     global_buffer
      - .actual_access:  read_only
        .address_space:  global
        .offset:         8
        .size:           8
        .value_kind:     global_buffer
      - .actual_access:  read_only
        .address_space:  global
        .offset:         16
        .size:           8
        .value_kind:     global_buffer
      - .actual_access:  write_only
        .address_space:  global
        .offset:         24
        .size:           8
        .value_kind:     global_buffer
    .group_segment_fixed_size: 0
    .kernarg_segment_align: 8
    .kernarg_segment_size: 32
    .language:       OpenCL C
    .language_version:
      - 2
      - 0
    .max_flat_workgroup_size: 256
    .name:           _Z9k_combinePKDF16_PK15HIP_vector_typeIiLj2EEPKS1_IfLj2EEPf
    .private_segment_fixed_size: 0
    .sgpr_count:     30
    .sgpr_spill_count: 0
    .symbol:         _Z9k_combinePKDF16_PK15HIP_vector_typeIiLj2EEPKS1_IfLj2EEPf.kd
    .uniform_work_group_size: 1
    .uses_dynamic_stack: false
    .vgpr_count:     64
    .vgpr_spill_count: 0
    .wavefront_size: 64
  - .agpr_count:     0
    .args:
      - .address_space:  global
        .offset:         0
        .size:           8
        .value_kind:     global_buffer
      - .address_space:  global
        .offset:         8
        .size:           8
        .value_kind:     global_buffer
      - .actual_access:  write_only
        .address_space:  global
        .offset:         16
        .size:           8
        .value_kind:     global_buffer
      - .actual_access:  read_only
        .address_space:  global
        .offset:         24
        .size:           8
        .value_kind:     global_buffer
      - .address_space:  global
        .offset:         32
        .size:           8
        .value_kind:     global_buffer
      - .address_space:  global
        .offset:         40
        .size:           8
        .value_kind:     global_buffer
      - .actual_access:  write_only
        .address_space:  global
        .offset:         48
        .size:           8
        .value_kind:     global_buffer
      - .address_space:  global
        .offset:         56
        .size:           8
        .value_kind:     global_buffer
    .group_segment_fixed_size: 0
    .kernarg_segment_align: 8
    .kernarg_segment_size: 64
    .language:       OpenCL C
    .language_version:
      - 2
      - 0
    .max_flat_workgroup_size: 512
    .name:           _Z7k_gemm1ILi0EEvPKDF16_S1_PDF16_PK15HIP_vector_typeIiLj2EEPKfS8_S2_PKt
    .private_segment_fixed_size: 0
    .sgpr_count:     108
    .sgpr_spill_count: 0
    .symbol:         _Z7k_gemm1ILi0EEvPKDF16_S1_PDF16_PK15HIP_vector_typeIiLj2EEPKfS8_S2_PKt.kd
    .uniform_work_group_size: 1
    .uses_dynamic_stack: false
    .vgpr_count:     256
    .vgpr_spill_count: 0
    .wavefront_size: 64
  - .agpr_count:     0
    .args:
      - .address_space:  global
        .offset:         0
        .size:           8
        .value_kind:     global_buffer
      - .address_space:  global
        .offset:         8
        .size:           8
        .value_kind:     global_buffer
      - .actual_access:  write_only
        .address_space:  global
        .offset:         16
        .size:           8
        .value_kind:     global_buffer
      - .actual_access:  read_only
        .address_space:  global
        .offset:         24
        .size:           8
        .value_kind:     global_buffer
      - .address_space:  global
        .offset:         32
        .size:           8
        .value_kind:     global_buffer
      - .actual_access:  read_only
        .address_space:  global
        .offset:         40
        .size:           8
        .value_kind:     global_buffer
      - .actual_access:  write_only
        .address_space:  global
        .offset:         48
        .size:           8
        .value_kind:     global_buffer
      - .address_space:  global
        .offset:         56
        .size:           8
        .value_kind:     global_buffer
    .group_segment_fixed_size: 0
    .kernarg_segment_align: 8
    .kernarg_segment_size: 64
    .language:       OpenCL C
    .language_version:
      - 2
      - 0
    .max_flat_workgroup_size: 512
    .name:           _Z7k_gemm1ILi1EEvPKDF16_S1_PDF16_PK15HIP_vector_typeIiLj2EEPKfS8_S2_PKt
    .private_segment_fixed_size: 0
    .sgpr_count:     100
    .sgpr_spill_count: 0
    .symbol:         _Z7k_gemm1ILi1EEvPKDF16_S1_PDF16_PK15HIP_vector_typeIiLj2EEPKfS8_S2_PKt.kd
    .uniform_work_group_size: 1
    .uses_dynamic_stack: false
    .vgpr_count:     254
    .vgpr_spill_count: 0
    .wavefront_size: 64
